# P2 QK-norm: 16-lane sum of squares via DPP adds instead of four serial ds_bpermute round trips per row
# baseline (speedup 1.0000x reference)
.LBB0_306:
	s_waitcnt lgkmcnt(0)
	global_load_dwordx4 v[0:3], v42, s[10:11] offset:16
	global_load_dwordx4 v[4:7], v42, s[10:11]
	v_add_u32_e32 v32, s26, v13
	s_lshr_b32 s98, s20, 26
	s_lshr_b32 s99, s26, 4
	s_and_b32 s98, s98, s99
	s_bfe_i32 s98, s98, 0x10000
	v_mbcnt_lo_u32_b32 v201, -1, 0
	v_mbcnt_hi_u32_b32 v201, -1, v201
	v_and_b32_e32 v201, 2, v201
	v_lshlrev_b32_e32 v201, 2, v201
	v_and_b32_e32 v202, s98, v201
	v_mov_b32_e32 v203, 0
	v_cvt_f32_fp8_e32 v49, v8
	v_cvt_f32_fp8_sdwa v62, v8 src0_sel:BYTE_1
	v_cvt_f32_fp8_sdwa v63, v8 src0_sel:BYTE_2
	v_cvt_f32_fp8_sdwa v64, v8 src0_sel:BYTE_3
	v_cvt_f32_fp8_e32 v65, v9
	v_cvt_f32_fp8_sdwa v66, v9 src0_sel:BYTE_1
	v_cvt_f32_fp8_sdwa v67, v9 src0_sel:BYTE_2
	v_cvt_f32_fp8_sdwa v68, v9 src0_sel:BYTE_3
	v_and_b32_e32 v8, 63, v32
	v_bfe_u32 v9, v32, 6, 8
	v_and_b32_e32 v11, 64, v41
	v_cndmask_b32_e64 v8, v8, v9, s[4:5]
	v_xor_b32_e32 v10, 1, v41
	v_add_u32_e32 v33, 64, v11
	v_lshlrev_b32_e32 v8, 7, v8
	v_mov_b32_e32 v9, v15
	v_cmp_lt_i32_e32 vcc, v10, v33
	v_lshl_add_u64 v[30:31], v[20:21], 0, v[8:9]
	v_lshl_add_u64 v[46:47], v[30:31], 0, v[14:15]
	v_cndmask_b32_e32 v10, v41, v10, vcc
	v_lshlrev_b32_e32 v45, 2, v10
	global_load_dwordx4 v[8:11], v[46:47], off offset:16
	global_load_dwordx4 v[50:53], v[46:47], off
	global_load_dwordx4 v[54:57], v[30:31], off offset:16
	global_load_dwordx4 v[58:61], v[30:31], off
	v_mul_f32_e32 v69, v62, v62
	v_fmac_f32_e32 v69, v49, v49
	v_fmac_f32_e32 v69, v63, v63
	v_fmac_f32_e32 v69, v64, v64
	v_fmac_f32_e32 v69, v65, v65
	v_fmac_f32_e32 v69, v66, v66
	v_fmac_f32_e32 v69, v67, v67
	v_fmac_f32_e32 v69, v68, v68
	s_nop 1
	v_xor_b32_e32 v48, 2, v41
	v_cmp_lt_i32_e32 vcc, v48, v33
	v_xor_b32_e32 v46, 4, v41
	s_nop 0
	v_cndmask_b32_e32 v30, v41, v48, vcc
	v_lshlrev_b32_e32 v47, 2, v30
	v_add_f32_dpp v30, v69, v69 quad_perm:[1,0,3,2] row_mask:0xf bank_mask:0xf
	s_nop 1
	v_cmp_lt_i32_e32 vcc, v46, v33
	v_xor_b32_e32 v48, 8, v41
	v_add_f32_dpp v30, v30, v30 quad_perm:[2,3,0,1] row_mask:0xf bank_mask:0xf
	v_cndmask_b32_e32 v46, v41, v46, vcc
	v_lshlrev_b32_e32 v46, 2, v46
	s_nop 1
	v_cmp_lt_i32_e32 vcc, v48, v33
	v_add_f32_dpp v30, v30, v30 row_half_mirror row_mask:0xf bank_mask:0xf
	v_cndmask_b32_e32 v33, v41, v48, vcc
	v_lshlrev_b32_e32 v48, 2, v33
	s_nop 1
	v_add_f32_dpp v30, v30, v30 row_mirror row_mask:0xf bank_mask:0xf
	v_fmamk_f32 v30, v30, 0x3c000000, v38
	v_mul_f32_e32 v31, 0x4f800000, v30
	v_cmp_gt_f32_e32 vcc, s1, v30
	s_nop 1
	v_cndmask_b32_e32 v30, v30, v31, vcc
	v_sqrt_f32_e32 v31, v30
	s_nop 0
	v_add_u32_e32 v33, -1, v31
	v_fma_f32 v69, -v33, v31, v30
	v_cmp_ge_f32_e64 s[10:11], 0, v69
	v_add_u32_e32 v69, 1, v31
	s_nop 0
	v_cndmask_b32_e64 v33, v31, v33, s[10:11]
	v_fma_f32 v31, -v69, v31, v30
	v_cmp_lt_f32_e64 s[10:11], 0, v31
	s_nop 1
	v_cndmask_b32_e64 v31, v33, v69, s[10:11]
	v_mul_f32_e32 v33, 0x37800000, v31
	v_cndmask_b32_e32 v31, v31, v33, vcc
	v_cmp_class_f32_e32 vcc, v30, v39
	s_nop 1
	v_cndmask_b32_e32 v33, v31, v30, vcc
	v_div_scale_f32 v69, s[10:11], v33, v33, 1.0
	v_rcp_f32_e32 v70, v69
	v_lshl_add_u64 v[30:31], v[22:23], 0, s[20:21]
	v_fma_f32 v71, -v69, v70, 1.0
	v_fmac_f32_e32 v70, v71, v70
	v_div_scale_f32 v71, vcc, 1.0, v33, 1.0
	v_mul_f32_e32 v72, v71, v70
	v_fma_f32 v73, -v69, v72, v71
	v_fmac_f32_e32 v72, v73, v70
	v_fma_f32 v69, -v69, v72, v71
	v_div_fmas_f32 v69, v69, v70, v72
	v_div_fixup_f32 v33, v69, v33, 1.0
	v_mul_f32_e32 v49, v49, v33
	s_waitcnt vmcnt(4)
	v_mul_f32_e32 v49, v4, v49
	ds_bpermute_b32 v69, v46, v49
	v_mul_f32_e32 v63, v63, v33
	v_mul_f32_e32 v63, v6, v63
	v_mul_f32_e32 v65, v65, v33
	v_mul_f32_e32 v65, v0, v65
	s_waitcnt vmcnt(2) lgkmcnt(0)
	v_mul_f32_e32 v50, v50, v69
	v_cndmask_b32_e64 v50, v50, -v50, s[6:7]
	s_waitcnt vmcnt(0)
	v_fmac_f32_e32 v50, v58, v49
	ds_bpermute_b32 v49, v46, v63
	v_mul_f32_e32 v64, v64, v33
	v_mul_f32_e32 v64, v7, v64
	ds_bpermute_b32 v58, v46, v64
	v_mul_f32_e32 v62, v62, v33
	s_waitcnt lgkmcnt(1)
	v_mul_f32_e32 v49, v52, v49
	ds_bpermute_b32 v52, v46, v65
	v_mul_f32_e32 v62, v5, v62
	v_mul_f32_e32 v67, v67, v33
	v_mul_f32_e32 v66, v66, v33
	v_mul_f32_e32 v67, v2, v67
	v_mul_f32_e32 v33, v68, v33
	ds_bpermute_b32 v68, v46, v62
	v_mul_f32_e32 v66, v1, v66
	s_waitcnt lgkmcnt(1)
	v_mul_f32_e32 v8, v8, v52
	ds_bpermute_b32 v52, v46, v67
	v_mul_f32_e32 v53, v53, v58
	ds_bpermute_b32 v58, v46, v66
	v_mul_f32_e32 v33, v3, v33
	s_waitcnt lgkmcnt(2)
	v_mul_f32_e32 v51, v51, v68
	v_cndmask_b32_e64 v51, v51, -v51, s[6:7]
	s_waitcnt lgkmcnt(1)
	v_mul_f32_e32 v10, v10, v52
	ds_bpermute_b32 v52, v46, v33
	v_fmac_f32_e32 v51, v59, v62
	s_waitcnt lgkmcnt(1)
	v_mul_f32_e32 v9, v9, v58
	v_cndmask_b32_e64 v8, v8, -v8, s[6:7]
	v_cndmask_b32_e64 v9, v9, -v9, s[6:7]
	v_mul_f32_e32 v50, s25, v50
	v_mul_f32_e32 v51, s25, v51
	v_fmac_f32_e32 v8, v54, v65
	v_fmac_f32_e32 v9, v55, v66
	v_med3_f32 v50, v50, s2, v40
	v_med3_f32 v51, v51, s2, v40
	v_mov_b32_e32 v54, v15
	v_cndmask_b32_e64 v49, v49, -v49, s[6:7]
	v_cndmask_b32_e64 v53, v53, -v53, s[6:7]
	v_cvt_pk_fp8_f32 v54, v50, v51
	v_mul_f32_e32 v8, s25, v8
	v_mul_f32_e32 v9, s25, v9
	v_fmac_f32_e32 v49, v60, v63
	v_fmac_f32_e32 v53, v61, v64
	s_waitcnt lgkmcnt(0)
	v_mul_f32_e32 v11, v11, v52
	v_med3_f32 v8, v8, s2, v40
	v_med3_f32 v9, v9, s2, v40
	v_mov_b32_e32 v51, v15
	v_cndmask_b32_e64 v10, v10, -v10, s[6:7]
	v_mul_f32_e32 v49, s25, v49
	v_mul_f32_e32 v50, s25, v53
	v_cndmask_b32_e64 v11, v11, -v11, s[6:7]
	v_cvt_pk_fp8_f32 v51, v8, v9
	v_fmac_f32_e32 v10, v56, v67
	v_med3_f32 v49, v49, s2, v40
	v_med3_f32 v50, v50, s2, v40
	v_fmac_f32_e32 v11, v57, v33
	v_cvt_pk_fp8_f32 v54, v49, v50 op_sel:[0,0,1]
	v_mul_f32_e32 v8, s25, v10
	v_mul_f32_e32 v9, s25, v11
	v_med3_f32 v8, v8, s2, v40
	v_med3_f32 v9, v9, s2, v40
	v_cvt_pk_fp8_f32 v51, v8, v9 op_sel:[0,0,1]
	v_lshrrev_b32_e32 v49, 2, v54
	v_and_b32_e32 v33, 0x1f1f1f1f, v54
	v_and_b32_e32 v49, 0x20202020, v49
	v_or_b32_e32 v50, v49, v33
	v_and_b32_e32 v9, 0x1f1f1f1f, v51
	v_lshrrev_b32_e32 v10, 2, v51
	v_bitop3_b32 v33, v49, 63, v33 bitop3:0xc8
	v_lshrrev_b32_e32 v49, 2, v50
	v_and_or_b32 v9, v10, s3, v9
	v_and_or_b32 v33, v49, s13, v33
	v_lshrrev_b32_e32 v49, 4, v50
	v_lshrrev_b32_e32 v8, 6, v50
	v_lshrrev_b32_e32 v10, 2, v9
	v_and_b32_e32 v49, 0x3f000, v49
	v_and_b32_e32 v8, 0xfc0000, v8
	v_and_b32_e32 v10, 0xfc0, v10
	v_or3_b32 v8, v33, v49, v8
	v_or_b32_e32 v11, v10, v9
	v_lshrrev_b32_e32 v33, 4, v9
	v_lshrrev_b32_e32 v9, 6, v9
	v_and_b32_e32 v33, 0x3f000, v33
	v_and_b32_e32 v9, 0xfc0000, v9
	v_or3_b32 v9, v33, v9, v10
	v_lshl_or_b32 v8, v11, 24, v8
	v_lshrrev_b32_e32 v9, 8, v9
	v_mov_b32_e32 v10, v15
	v_mov_b32_e32 v11, v15
	s_nop 0
	v_mov_b32_dpp v10, v8 quad_perm:[1,0,3,2] row_mask:0xf bank_mask:0xf
	v_mov_b32_dpp v11, v9 quad_perm:[1,0,3,2] row_mask:0xf bank_mask:0xf
	s_and_saveexec_b64 s[10:11], s[8:9]
	s_cbranch_execz .LBB0_308
	v_ashrrev_i32_e32 v33, 31, v32
	v_lshlrev_b64 v[50:51], 7, v[32:33]
	v_lshl_add_u64 v[50:51], v[30:31], 0, v[50:51]
	v_lshl_or_b32 v9, v10, 16, v9
	v_perm_b32 v10, v10, v11, s15
	global_store_dword v[50:51], v8, off
	v_lshl_add_u64 v[204:205], v[50:51], 0, v[202:203]
	global_store_dword v[204:205], v9, off offset:4
	global_store_dword v[204:205], v10, off offset:8
.LBB0_308:
	s_or_b64 exec, exec, s[10:11]
	v_cvt_f32_fp8_sdwa v33, v36 src0_sel:BYTE_1
	v_cvt_f32_fp8_e32 v11, v36
	v_cvt_f32_fp8_sdwa v49, v36 src0_sel:BYTE_2
	v_cvt_f32_fp8_sdwa v66, v36 src0_sel:BYTE_3
	v_cvt_f32_fp8_e32 v67, v37
	v_mul_f32_e32 v58, v33, v33
	v_cvt_f32_fp8_sdwa v68, v37 src0_sel:BYTE_1
	v_fmac_f32_e32 v58, v11, v11
	v_cvt_f32_fp8_sdwa v69, v37 src0_sel:BYTE_2
	v_fmac_f32_e32 v58, v49, v49
	v_add_u32_e32 v10, 4, v32
	v_cvt_f32_fp8_sdwa v70, v37 src0_sel:BYTE_3
	v_fmac_f32_e32 v58, v66, v66
	v_and_b32_e32 v8, 63, v10
	v_bfe_u32 v9, v10, 6, 8
	v_fmac_f32_e32 v58, v67, v67
	v_cndmask_b32_e64 v8, v8, v9, s[4:5]
	v_fmac_f32_e32 v58, v68, v68
	v_lshlrev_b32_e32 v8, 7, v8
	v_mov_b32_e32 v9, v15
	v_fmac_f32_e32 v58, v69, v69
	v_lshl_add_u64 v[8:9], v[20:21], 0, v[8:9]
	v_fmac_f32_e32 v58, v70, v70
	v_lshl_add_u64 v[36:37], v[8:9], 0, v[14:15]
	global_load_dwordx4 v[50:53], v[36:37], off
	global_load_dwordx4 v[54:57], v[8:9], off
	s_nop 1
	v_add_f32_dpp v58, v58, v58 quad_perm:[1,0,3,2] row_mask:0xf bank_mask:0xf
	s_nop 1
	v_add_f32_dpp v71, v58, v58 quad_perm:[2,3,0,1] row_mask:0xf bank_mask:0xf
	global_load_dwordx4 v[58:61], v[36:37], off offset:16
	global_load_dwordx4 v[62:65], v[8:9], off offset:16
	s_nop 1
	v_add_f32_dpp v8, v71, v71 row_half_mirror row_mask:0xf bank_mask:0xf
	s_nop 1
	v_add_f32_dpp v8, v8, v8 row_mirror row_mask:0xf bank_mask:0xf
	v_fmamk_f32 v8, v8, 0x3c000000, v38
	v_mul_f32_e32 v9, 0x4f800000, v8
	v_cmp_gt_f32_e32 vcc, s1, v8
	s_nop 1
	v_cndmask_b32_e32 v8, v8, v9, vcc
	v_sqrt_f32_e32 v9, v8
	s_nop 0
	v_add_u32_e32 v36, -1, v9
	v_fma_f32 v71, -v36, v9, v8
	v_add_u32_e32 v37, 1, v9
	v_cmp_ge_f32_e64 s[10:11], 0, v71
	s_nop 1
	v_cndmask_b32_e64 v36, v9, v36, s[10:11]
	v_fma_f32 v9, -v37, v9, v8
	v_cmp_lt_f32_e64 s[10:11], 0, v9
	s_nop 1
	v_cndmask_b32_e64 v9, v36, v37, s[10:11]
	v_mul_f32_e32 v36, 0x37800000, v9
	v_cndmask_b32_e32 v9, v9, v36, vcc
	v_cmp_class_f32_e32 vcc, v8, v39
	s_nop 1
	v_cndmask_b32_e32 v8, v9, v8, vcc
	v_div_scale_f32 v9, s[10:11], v8, v8, 1.0
	v_rcp_f32_e32 v36, v9
	v_div_scale_f32 v37, vcc, 1.0, v8, 1.0
	v_fma_f32 v71, -v9, v36, 1.0
	v_fmac_f32_e32 v36, v71, v36
	v_mul_f32_e32 v71, v37, v36
	v_fma_f32 v72, -v9, v71, v37
	v_fmac_f32_e32 v71, v72, v36
	v_fma_f32 v9, -v9, v71, v37
	v_div_fmas_f32 v9, v9, v36, v71
	v_div_fixup_f32 v8, v9, v8, 1.0
	v_mul_f32_e32 v9, v11, v8
	v_mul_f32_e32 v9, v4, v9
	v_mul_f32_e32 v11, v67, v8
	v_mul_f32_e32 v33, v33, v8
	ds_bpermute_b32 v67, v46, v9
	v_mul_f32_e32 v37, v49, v8
	v_mul_f32_e32 v33, v5, v33
	v_mul_f32_e32 v36, v68, v8
	v_mul_f32_e32 v37, v6, v37
	ds_bpermute_b32 v68, v46, v33
	v_mul_f32_e32 v49, v69, v8
	ds_bpermute_b32 v69, v46, v37
	s_waitcnt vmcnt(3) lgkmcnt(2)
	v_mul_f32_e32 v50, v50, v67
	v_cndmask_b32_e64 v50, v50, -v50, s[6:7]
	v_mul_f32_e32 v66, v66, v8
	s_waitcnt vmcnt(2)
	v_fmac_f32_e32 v50, v54, v9
	s_waitcnt lgkmcnt(1)
	v_mul_f32_e32 v9, v51, v68
	v_mul_f32_e32 v66, v7, v66
	v_cndmask_b32_e64 v9, v9, -v9, s[6:7]
	s_waitcnt lgkmcnt(0)
	v_mul_f32_e32 v51, v52, v69
	v_mul_f32_e32 v11, v0, v11
	v_fmac_f32_e32 v9, v55, v33
	ds_bpermute_b32 v33, v46, v66
	v_cndmask_b32_e64 v51, v51, -v51, s[6:7]
	v_fmac_f32_e32 v51, v56, v37
	ds_bpermute_b32 v37, v46, v11
	v_mul_f32_e32 v36, v1, v36
	ds_bpermute_b32 v52, v46, v36
	v_mul_f32_e32 v49, v2, v49
	s_waitcnt lgkmcnt(2)
	v_mul_f32_e32 v33, v53, v33
	ds_bpermute_b32 v53, v46, v49
	s_waitcnt vmcnt(1) lgkmcnt(2)
	v_mul_f32_e32 v37, v58, v37
	v_cndmask_b32_e64 v37, v37, -v37, s[6:7]
	s_waitcnt vmcnt(0)
	v_fmac_f32_e32 v37, v62, v11
	s_waitcnt lgkmcnt(1)
	v_mul_f32_e32 v11, v59, v52
	v_cndmask_b32_e64 v11, v11, -v11, s[6:7]
	v_mul_f32_e32 v8, v70, v8
	v_fmac_f32_e32 v11, v63, v36
	s_waitcnt lgkmcnt(0)
	v_mul_f32_e32 v36, v60, v53
	v_mul_f32_e32 v50, s25, v50
	v_mul_f32_e32 v9, s25, v9
	v_mul_f32_e32 v8, v3, v8
	v_cndmask_b32_e64 v36, v36, -v36, s[6:7]
	v_med3_f32 v50, v50, s2, v40
	v_med3_f32 v9, v9, s2, v40
	v_mov_b32_e32 v52, v15
	v_cndmask_b32_e64 v33, v33, -v33, s[6:7]
	v_fmac_f32_e32 v36, v64, v49
	ds_bpermute_b32 v49, v46, v8
	v_cvt_pk_fp8_f32 v52, v50, v9
	v_fmac_f32_e32 v33, v57, v66
	v_mul_f32_e32 v9, s25, v51
	v_mul_f32_e32 v33, s25, v33
	v_med3_f32 v9, v9, s2, v40
	v_med3_f32 v33, v33, s2, v40
	v_cvt_pk_fp8_f32 v52, v9, v33 op_sel:[0,0,1]
	v_mul_f32_e32 v37, s25, v37
	v_mul_f32_e32 v11, s25, v11
	s_waitcnt lgkmcnt(0)
	v_mul_f32_e32 v9, v61, v49
	v_med3_f32 v37, v37, s2, v40
	v_med3_f32 v11, v11, s2, v40
	v_mov_b32_e32 v50, v15
	v_cndmask_b32_e64 v9, v9, -v9, s[6:7]
	v_cvt_pk_fp8_f32 v50, v37, v11
	v_fmac_f32_e32 v9, v65, v8
	v_lshrrev_b32_e32 v33, 2, v52
	v_mul_f32_e32 v11, s25, v36
	v_mul_f32_e32 v9, s25, v9
	v_and_b32_e32 v8, 0x1f1f1f1f, v52
	v_and_b32_e32 v33, 0x20202020, v33
	v_med3_f32 v11, v11, s2, v40
	v_med3_f32 v9, v9, s2, v40
	v_or_b32_e32 v49, v33, v8
	v_cvt_pk_fp8_f32 v50, v11, v9 op_sel:[0,0,1]
	v_bitop3_b32 v8, v33, 63, v8 bitop3:0xc8
	v_lshrrev_b32_e32 v33, 2, v49
	v_and_or_b32 v8, v33, s13, v8
	v_lshrrev_b32_e32 v33, 4, v49
	v_lshrrev_b32_e32 v9, 6, v49
	v_and_b32_e32 v33, 0x3f000, v33
	v_and_b32_e32 v9, 0xfc0000, v9
	v_or3_b32 v8, v8, v33, v9
	v_and_b32_e32 v9, 0x1f1f1f1f, v50
	v_lshrrev_b32_e32 v11, 2, v50
	v_and_or_b32 v9, v11, s3, v9
	v_lshrrev_b32_e32 v11, 2, v9
	v_and_b32_e32 v11, 0xfc0, v11
	v_or_b32_e32 v33, v11, v9
	v_lshrrev_b32_e32 v36, 4, v9
	v_lshrrev_b32_e32 v9, 6, v9
	v_and_b32_e32 v36, 0x3f000, v36
	v_and_b32_e32 v9, 0xfc0000, v9
	v_or3_b32 v9, v36, v9, v11
	v_lshl_or_b32 v8, v33, 24, v8
	v_lshrrev_b32_e32 v9, 8, v9
	v_mov_b32_e32 v33, v15
	v_mov_b32_e32 v36, v15
	s_nop 0
	v_mov_b32_dpp v33, v8 quad_perm:[1,0,3,2] row_mask:0xf bank_mask:0xf
	v_mov_b32_dpp v36, v9 quad_perm:[1,0,3,2] row_mask:0xf bank_mask:0xf
	s_and_saveexec_b64 s[10:11], s[8:9]
	s_cbranch_execz .LBB0_310
	v_ashrrev_i32_e32 v11, 31, v10
	v_lshlrev_b64 v[10:11], 7, v[10:11]
	v_lshl_add_u64 v[50:51], v[30:31], 0, v[10:11]
	v_lshl_or_b32 v9, v33, 16, v9
	v_perm_b32 v10, v33, v36, s15
	global_store_dword v[50:51], v8, off
	v_lshl_add_u64 v[204:205], v[50:51], 0, v[202:203]
	global_store_dword v[204:205], v9, off offset:4
	global_store_dword v[204:205], v10, off offset:8
.LBB0_310:
	s_or_b64 exec, exec, s[10:11]
	v_cvt_f32_fp8_sdwa v33, v34 src0_sel:BYTE_1
	v_cvt_f32_fp8_e32 v11, v34
	v_cvt_f32_fp8_sdwa v49, v34 src0_sel:BYTE_2
	v_cvt_f32_fp8_sdwa v64, v34 src0_sel:BYTE_3
	v_cvt_f32_fp8_e32 v65, v35
	v_mul_f32_e32 v54, v33, v33
	v_add_u32_e32 v10, 8, v32
	v_cvt_f32_fp8_sdwa v66, v35 src0_sel:BYTE_1
	v_fmac_f32_e32 v54, v11, v11
	v_and_b32_e32 v8, 63, v10
	v_bfe_u32 v9, v10, 6, 8
	v_cvt_f32_fp8_sdwa v67, v35 src0_sel:BYTE_2
	v_fmac_f32_e32 v54, v49, v49
	v_cndmask_b32_e64 v8, v8, v9, s[4:5]
	v_cvt_f32_fp8_sdwa v68, v35 src0_sel:BYTE_3
	v_fmac_f32_e32 v54, v64, v64
	v_lshlrev_b32_e32 v8, 7, v8
	v_mov_b32_e32 v9, v15
	v_fmac_f32_e32 v54, v65, v65
	v_lshl_add_u64 v[8:9], v[20:21], 0, v[8:9]
	v_fmac_f32_e32 v54, v66, v66
	v_lshl_add_u64 v[62:63], v[8:9], 0, v[14:15]
	v_fmac_f32_e32 v54, v67, v67
	global_load_dwordx4 v[34:37], v[62:63], off
	global_load_dwordx4 v[50:53], v[8:9], off
	v_fmac_f32_e32 v54, v68, v68
	s_nop 1
	v_add_f32_dpp v54, v54, v54 quad_perm:[1,0,3,2] row_mask:0xf bank_mask:0xf
	s_nop 1
	v_add_f32_dpp v69, v54, v54 quad_perm:[2,3,0,1] row_mask:0xf bank_mask:0xf
	global_load_dwordx4 v[54:57], v[62:63], off offset:16
	global_load_dwordx4 v[58:61], v[8:9], off offset:16
	s_nop 1
	v_add_f32_dpp v8, v69, v69 row_half_mirror row_mask:0xf bank_mask:0xf
	s_nop 1
	v_add_f32_dpp v8, v8, v8 row_mirror row_mask:0xf bank_mask:0xf
	v_fmamk_f32 v8, v8, 0x3c000000, v38
	v_mul_f32_e32 v9, 0x4f800000, v8
	v_cmp_gt_f32_e32 vcc, s1, v8
	s_nop 1
	v_cndmask_b32_e32 v8, v8, v9, vcc
	v_sqrt_f32_e32 v9, v8
	s_nop 0
	v_add_u32_e32 v62, -1, v9
	v_fma_f32 v69, -v62, v9, v8
	v_add_u32_e32 v63, 1, v9
	v_cmp_ge_f32_e64 s[10:11], 0, v69
	s_nop 1
	v_cndmask_b32_e64 v62, v9, v62, s[10:11]
	v_fma_f32 v9, -v63, v9, v8
	v_cmp_lt_f32_e64 s[10:11], 0, v9
	s_nop 1
	v_cndmask_b32_e64 v9, v62, v63, s[10:11]
	v_mul_f32_e32 v62, 0x37800000, v9
	v_cndmask_b32_e32 v9, v9, v62, vcc
	v_cmp_class_f32_e32 vcc, v8, v39
	s_nop 1
	v_cndmask_b32_e32 v8, v9, v8, vcc
	v_div_scale_f32 v9, s[10:11], v8, v8, 1.0
	v_rcp_f32_e32 v62, v9
	v_div_scale_f32 v63, vcc, 1.0, v8, 1.0
	v_fma_f32 v69, -v9, v62, 1.0
	v_fmac_f32_e32 v62, v69, v62
	v_mul_f32_e32 v69, v63, v62
	v_fma_f32 v70, -v9, v69, v63
	v_fmac_f32_e32 v69, v70, v62
	v_fma_f32 v9, -v9, v69, v63
	v_div_fmas_f32 v9, v9, v62, v69
	v_div_fixup_f32 v8, v9, v8, 1.0
	v_mul_f32_e32 v9, v11, v8
	v_mul_f32_e32 v9, v4, v9
	v_mul_f32_e32 v11, v65, v8
	v_mul_f32_e32 v33, v33, v8
	ds_bpermute_b32 v65, v46, v9
	v_mul_f32_e32 v33, v5, v33
	v_mul_f32_e32 v62, v66, v8
	ds_bpermute_b32 v66, v46, v33
	v_mul_f32_e32 v49, v49, v8
	v_mul_f32_e32 v49, v6, v49
	s_waitcnt vmcnt(3) lgkmcnt(1)
	v_mul_f32_e32 v34, v34, v65
	v_cndmask_b32_e64 v34, v34, -v34, s[6:7]
	v_mul_f32_e32 v63, v67, v8
	v_mul_f32_e32 v64, v64, v8
	ds_bpermute_b32 v67, v46, v49
	s_waitcnt vmcnt(2)
	v_fmac_f32_e32 v34, v50, v9
	s_waitcnt lgkmcnt(1)
	v_mul_f32_e32 v9, v35, v66
	v_mul_f32_e32 v64, v7, v64
	v_cndmask_b32_e64 v9, v9, -v9, s[6:7]
	v_fmac_f32_e32 v9, v51, v33
	ds_bpermute_b32 v33, v46, v64
	v_mul_f32_e32 v11, v0, v11
	s_waitcnt lgkmcnt(1)
	v_mul_f32_e32 v35, v36, v67
	ds_bpermute_b32 v36, v46, v11
	v_mul_f32_e32 v62, v1, v62
	v_mul_f32_e32 v63, v2, v63
	v_cndmask_b32_e64 v35, v35, -v35, s[6:7]
	v_fmac_f32_e32 v35, v52, v49
	s_waitcnt lgkmcnt(1)
	v_mul_f32_e32 v33, v37, v33
	ds_bpermute_b32 v37, v46, v62
	ds_bpermute_b32 v49, v46, v63
	v_mul_f32_e32 v8, v68, v8
	s_waitcnt vmcnt(1) lgkmcnt(2)
	v_mul_f32_e32 v36, v54, v36
	v_mul_f32_e32 v34, s25, v34
	v_mul_f32_e32 v9, s25, v9
	v_mul_f32_e32 v8, v3, v8
	v_cndmask_b32_e64 v36, v36, -v36, s[6:7]
	v_med3_f32 v34, v34, s2, v40
	v_med3_f32 v9, v9, s2, v40
	v_mov_b32_e32 v50, v15
	v_cndmask_b32_e64 v33, v33, -v33, s[6:7]
	s_waitcnt vmcnt(0)
	v_fmac_f32_e32 v36, v58, v11
	s_waitcnt lgkmcnt(1)
	v_mul_f32_e32 v11, v55, v37
	s_waitcnt lgkmcnt(0)
	v_mul_f32_e32 v37, v56, v49
	ds_bpermute_b32 v49, v46, v8
	v_cvt_pk_fp8_f32 v50, v34, v9
	v_fmac_f32_e32 v33, v53, v64
	v_cndmask_b32_e64 v11, v11, -v11, s[6:7]
	v_mul_f32_e32 v9, s25, v35
	v_mul_f32_e32 v33, s25, v33
	v_fmac_f32_e32 v11, v59, v62
	v_med3_f32 v9, v9, s2, v40
	v_med3_f32 v33, v33, s2, v40
	v_cvt_pk_fp8_f32 v50, v9, v33 op_sel:[0,0,1]
	v_mul_f32_e32 v35, s25, v36
	v_mul_f32_e32 v11, s25, v11
	s_waitcnt lgkmcnt(0)
	v_mul_f32_e32 v9, v57, v49
	v_med3_f32 v35, v35, s2, v40
	v_med3_f32 v11, v11, s2, v40
	v_mov_b32_e32 v36, v15
	v_cndmask_b32_e64 v37, v37, -v37, s[6:7]
	v_cndmask_b32_e64 v9, v9, -v9, s[6:7]
	v_cvt_pk_fp8_f32 v36, v35, v11
	v_fmac_f32_e32 v37, v60, v63
	v_fmac_f32_e32 v9, v61, v8
	v_lshrrev_b32_e32 v33, 2, v50
	v_mul_f32_e32 v11, s25, v37
	v_mul_f32_e32 v9, s25, v9
	v_and_b32_e32 v8, 0x1f1f1f1f, v50
	v_and_b32_e32 v33, 0x20202020, v33
	v_med3_f32 v11, v11, s2, v40
	v_med3_f32 v9, v9, s2, v40
	v_or_b32_e32 v34, v33, v8
	v_cvt_pk_fp8_f32 v36, v11, v9 op_sel:[0,0,1]
	v_bitop3_b32 v8, v33, 63, v8 bitop3:0xc8
	v_lshrrev_b32_e32 v33, 2, v34
	v_and_or_b32 v8, v33, s13, v8
	v_lshrrev_b32_e32 v33, 4, v34
	v_lshrrev_b32_e32 v9, 6, v34
	v_and_b32_e32 v33, 0x3f000, v33
	v_and_b32_e32 v9, 0xfc0000, v9
	v_or3_b32 v8, v8, v33, v9
	v_and_b32_e32 v9, 0x1f1f1f1f, v36
	v_lshrrev_b32_e32 v11, 2, v36
	v_and_or_b32 v9, v11, s3, v9
	v_lshrrev_b32_e32 v11, 2, v9
	v_and_b32_e32 v11, 0xfc0, v11
	v_or_b32_e32 v33, v11, v9
	v_lshrrev_b32_e32 v34, 4, v9
	v_lshrrev_b32_e32 v9, 6, v9
	v_and_b32_e32 v34, 0x3f000, v34
	v_and_b32_e32 v9, 0xfc0000, v9
	v_or3_b32 v9, v34, v9, v11
	v_lshl_or_b32 v8, v33, 24, v8
	v_lshrrev_b32_e32 v9, 8, v9
	v_mov_b32_e32 v33, v15
	v_mov_b32_e32 v34, v15
	s_nop 0
	v_mov_b32_dpp v33, v8 quad_perm:[1,0,3,2] row_mask:0xf bank_mask:0xf
	v_mov_b32_dpp v34, v9 quad_perm:[1,0,3,2] row_mask:0xf bank_mask:0xf
	s_and_saveexec_b64 s[10:11], s[8:9]
	s_cbranch_execz .LBB0_312
	v_ashrrev_i32_e32 v11, 31, v10
	v_lshlrev_b64 v[10:11], 7, v[10:11]
	v_lshl_add_u64 v[36:37], v[30:31], 0, v[10:11]
	v_lshl_or_b32 v9, v33, 16, v9
	v_perm_b32 v10, v33, v34, s15
	global_store_dword v[36:37], v8, off
	v_lshl_add_u64 v[204:205], v[36:37], 0, v[202:203]
	global_store_dword v[204:205], v9, off offset:4
	global_store_dword v[204:205], v10, off offset:8
.LBB0_312:
	s_or_b64 exec, exec, s[10:11]
	s_nop 0
	v_add_u32_e32 v8, 12, v32
	v_and_b32_e32 v10, 63, v8
	v_bfe_u32 v11, v8, 6, 8
	v_cndmask_b32_e64 v10, v10, v11, s[4:5]
	v_lshlrev_b32_e32 v10, 7, v10
	v_mov_b32_e32 v11, v15
	v_cvt_f32_fp8_sdwa v49, v44 src0_sel:BYTE_1
	v_lshl_add_u64 v[10:11], v[20:21], 0, v[10:11]
	v_cvt_f32_fp8_e32 v9, v44
	v_lshl_add_u64 v[36:37], v[10:11], 0, v[14:15]
	v_cvt_f32_fp8_sdwa v62, v44 src0_sel:BYTE_2
	global_load_dwordx4 v[32:35], v[36:37], off
	global_load_dwordx4 v[50:53], v[10:11], off
	v_cvt_f32_fp8_sdwa v44, v44 src0_sel:BYTE_3
	v_cvt_f32_fp8_e32 v63, v43
	v_mul_f32_e32 v54, v49, v49
	v_cvt_f32_fp8_sdwa v64, v43 src0_sel:BYTE_1
	v_fmac_f32_e32 v54, v9, v9
	v_cvt_f32_fp8_sdwa v65, v43 src0_sel:BYTE_2
	v_fmac_f32_e32 v54, v62, v62
	v_cvt_f32_fp8_sdwa v43, v43 src0_sel:BYTE_3
	v_fmac_f32_e32 v54, v44, v44
	v_fmac_f32_e32 v54, v63, v63
	v_fmac_f32_e32 v54, v64, v64
	v_fmac_f32_e32 v54, v65, v65
	v_fmac_f32_e32 v54, v43, v43
	s_nop 1
	v_add_f32_dpp v45, v54, v54 quad_perm:[1,0,3,2] row_mask:0xf bank_mask:0xf
	global_load_dwordx4 v[54:57], v[36:37], off offset:16
	global_load_dwordx4 v[58:61], v[10:11], off offset:16
	s_nop 1
	v_add_f32_dpp v45, v45, v45 quad_perm:[2,3,0,1] row_mask:0xf bank_mask:0xf
	s_nop 1
	v_add_f32_dpp v10, v45, v45 row_half_mirror row_mask:0xf bank_mask:0xf
	s_nop 1
	v_add_f32_dpp v10, v10, v10 row_mirror row_mask:0xf bank_mask:0xf
	v_fmamk_f32 v10, v10, 0x3c000000, v38
	v_mul_f32_e32 v11, 0x4f800000, v10
	v_cmp_gt_f32_e32 vcc, s1, v10
	s_nop 1
	v_cndmask_b32_e32 v10, v10, v11, vcc
	v_sqrt_f32_e32 v11, v10
	s_nop 0
	v_add_u32_e32 v36, -1, v11
	v_fma_f32 v45, -v36, v11, v10
	v_add_u32_e32 v37, 1, v11
	v_cmp_ge_f32_e64 s[10:11], 0, v45
	s_nop 1
	v_cndmask_b32_e64 v36, v11, v36, s[10:11]
	v_fma_f32 v11, -v37, v11, v10
	v_cmp_lt_f32_e64 s[10:11], 0, v11
	s_nop 1
	v_cndmask_b32_e64 v11, v36, v37, s[10:11]
	v_mul_f32_e32 v36, 0x37800000, v11
	v_cndmask_b32_e32 v11, v11, v36, vcc
	v_cmp_class_f32_e32 vcc, v10, v39
	s_nop 1
	v_cndmask_b32_e32 v10, v11, v10, vcc
	v_div_scale_f32 v11, s[10:11], v10, v10, 1.0
	v_rcp_f32_e32 v36, v11
	v_div_scale_f32 v37, vcc, 1.0, v10, 1.0
	v_fma_f32 v45, -v11, v36, 1.0
	v_fmac_f32_e32 v36, v45, v36
	v_mul_f32_e32 v45, v37, v36
	v_fma_f32 v47, -v11, v45, v37
	v_fmac_f32_e32 v45, v47, v36
	v_fma_f32 v11, -v11, v45, v37
	v_div_fmas_f32 v11, v11, v36, v45
	v_div_fixup_f32 v10, v11, v10, 1.0
	v_mul_f32_e32 v9, v9, v10
	v_mul_f32_e32 v4, v4, v9
	v_mul_f32_e32 v36, v49, v10
	ds_bpermute_b32 v9, v46, v4
	v_mul_f32_e32 v11, v63, v10
	v_mul_f32_e32 v37, v64, v10
	v_mul_f32_e32 v45, v62, v10
	v_mul_f32_e32 v47, v65, v10
	v_mul_f32_e32 v44, v44, v10
	v_mul_f32_e32 v10, v43, v10
	v_mul_f32_e32 v5, v5, v36
	v_mul_f32_e32 v3, v3, v10
	ds_bpermute_b32 v10, v46, v5
	s_waitcnt vmcnt(3) lgkmcnt(1)
	v_mul_f32_e32 v9, v32, v9
	v_mul_f32_e32 v6, v6, v45
	v_cndmask_b32_e64 v9, v9, -v9, s[6:7]
	v_mul_f32_e32 v0, v0, v11
	ds_bpermute_b32 v11, v46, v6
	s_waitcnt vmcnt(2)
	v_fmac_f32_e32 v9, v50, v4
	s_waitcnt lgkmcnt(1)
	v_mul_f32_e32 v4, v33, v10
	v_mul_f32_e32 v7, v7, v44
	v_cndmask_b32_e64 v4, v4, -v4, s[6:7]
	v_fmac_f32_e32 v4, v51, v5
	ds_bpermute_b32 v5, v46, v7
	s_waitcnt lgkmcnt(1)
	v_mul_f32_e32 v10, v34, v11
	v_cndmask_b32_e64 v10, v10, -v10, s[6:7]
	v_fmac_f32_e32 v10, v52, v6
	ds_bpermute_b32 v6, v46, v0
	s_waitcnt lgkmcnt(1)
	v_mul_f32_e32 v5, v35, v5
	v_mul_f32_e32 v1, v1, v37
	v_cndmask_b32_e64 v5, v5, -v5, s[6:7]
	v_fmac_f32_e32 v5, v53, v7
	ds_bpermute_b32 v7, v46, v1
	v_mul_f32_e32 v2, v2, v47
	ds_bpermute_b32 v11, v46, v2
	s_waitcnt vmcnt(1) lgkmcnt(2)
	v_mul_f32_e32 v6, v54, v6
	v_cndmask_b32_e64 v6, v6, -v6, s[6:7]
	s_waitcnt vmcnt(0)
	v_fmac_f32_e32 v6, v58, v0
	s_waitcnt lgkmcnt(1)
	v_mul_f32_e32 v0, v55, v7
	v_cndmask_b32_e64 v0, v0, -v0, s[6:7]
	v_fmac_f32_e32 v0, v59, v1
	s_waitcnt lgkmcnt(0)
	v_mul_f32_e32 v1, v56, v11
	v_cndmask_b32_e64 v1, v1, -v1, s[6:7]
	v_fmac_f32_e32 v1, v60, v2
	ds_bpermute_b32 v2, v46, v3
	v_mul_f32_e32 v7, s25, v9
	v_mul_f32_e32 v4, s25, v4
	v_med3_f32 v7, v7, s2, v40
	v_med3_f32 v4, v4, s2, v40
	v_mov_b32_e32 v9, v15
	v_cvt_pk_fp8_f32 v9, v7, v4
	v_mul_f32_e32 v6, s25, v6
	v_mul_f32_e32 v0, s25, v0
	s_waitcnt lgkmcnt(0)
	v_mul_f32_e32 v2, v57, v2
	v_med3_f32 v6, v6, s2, v40
	v_med3_f32 v0, v0, s2, v40
	v_mov_b32_e32 v7, v15
	v_mul_f32_e32 v4, s25, v10
	v_mul_f32_e32 v5, s25, v5
	v_cndmask_b32_e64 v2, v2, -v2, s[6:7]
	v_cvt_pk_fp8_f32 v7, v6, v0
	v_med3_f32 v4, v4, s2, v40
	v_med3_f32 v5, v5, s2, v40
	v_fmac_f32_e32 v2, v61, v3
	v_cvt_pk_fp8_f32 v9, v4, v5 op_sel:[0,0,1]
	v_mul_f32_e32 v0, s25, v1
	v_mul_f32_e32 v1, s25, v2
	v_med3_f32 v0, v0, s2, v40
	v_med3_f32 v1, v1, s2, v40
	v_cvt_pk_fp8_f32 v7, v0, v1 op_sel:[0,0,1]
	v_lshrrev_b32_e32 v4, 2, v9
	v_and_b32_e32 v3, 0x1f1f1f1f, v9
	v_and_b32_e32 v4, 0x20202020, v4
	v_or_b32_e32 v5, v4, v3
	v_and_b32_e32 v1, 0x1f1f1f1f, v7
	v_lshrrev_b32_e32 v2, 2, v7
	v_bitop3_b32 v3, v4, 63, v3 bitop3:0xc8
	v_lshrrev_b32_e32 v4, 2, v5
	v_and_or_b32 v1, v2, s3, v1
	v_and_or_b32 v3, v4, s13, v3
	v_lshrrev_b32_e32 v4, 4, v5
	v_lshrrev_b32_e32 v0, 6, v5
	v_lshrrev_b32_e32 v2, 2, v1
	v_and_b32_e32 v4, 0x3f000, v4
	v_and_b32_e32 v0, 0xfc0000, v0
	v_and_b32_e32 v2, 0xfc0, v2
	v_or3_b32 v0, v3, v4, v0
	v_or_b32_e32 v3, v2, v1
	v_lshrrev_b32_e32 v4, 4, v1
	v_lshrrev_b32_e32 v1, 6, v1
	v_and_b32_e32 v4, 0x3f000, v4
	v_and_b32_e32 v1, 0xfc0000, v1
	v_or3_b32 v1, v4, v1, v2
	v_lshl_or_b32 v0, v3, 24, v0
	v_lshrrev_b32_e32 v1, 8, v1
	v_mov_b32_e32 v2, v15
	v_mov_b32_e32 v3, v15
	s_nop 0
	v_mov_b32_dpp v2, v0 quad_perm:[1,0,3,2] row_mask:0xf bank_mask:0xf
	v_mov_b32_dpp v3, v1 quad_perm:[1,0,3,2] row_mask:0xf bank_mask:0xf
	s_and_saveexec_b64 s[10:11], s[8:9]
	s_cbranch_execz .LBB0_298
	v_ashrrev_i32_e32 v9, 31, v8
	v_lshlrev_b64 v[4:5], 7, v[8:9]
	v_lshl_add_u64 v[4:5], v[30:31], 0, v[4:5]
	v_lshl_or_b32 v1, v2, 16, v1
	v_perm_b32 v2, v2, v3, s15
	global_store_dword v[4:5], v0, off
	v_lshl_add_u64 v[204:205], v[4:5], 0, v[202:203]
	global_store_dword v[204:205], v1, off offset:4
	global_store_dword v[204:205], v2, off offset:8
	s_branch .LBB0_298
